# peersel: redundant top-of-unit barrier removed (waves that do not run the last stage start the next unit's MFMA stage early)
# speedup vs baseline: 1.0050x; 1.0050x over previous
; #define MFMA16(a, b, c) __builtin_amdgcn_mfma_f32_16x16x32_bf16((a), (b), (c), 0, 0, 0)
; DI void peer_select_unit(const Params& p, int unit, char* lds, const bf16x8 (&kb)[4][4]) {
;     ...
;   __syncthreads();
;   {
;     const int set = wid >> 1, kh = wid & 1;
;     bf16x8 qa[2][4];
; #pragma unroll
;     for (int mt = 0; mt < 2; ++mt)
; #pragma unroll
;       for (int kk = 0; kk < 4; ++kk) qa[mt][kk] = *(const bf16x8*)(qy + (size_t)(t0 + 16 * mt + fr) * 2048 + h * 256 + set * 128 + kk * 32 + fq * 8);
; #pragma unroll
;     for (int mt = 0; mt < 2; ++mt)
; #pragma unroll
;       for (int nj = 0; nj < 4; ++nj) {
;         f32x4 d = {0.f, 0.f, 0.f, 0.f};
; #pragma unroll
;         for (int kk = 0; kk < 4; ++kk) d = MFMA16(qa[mt][kk], kb[nj][kk], d);
; #pragma unroll
;         for (int r = 0; r < 4; ++r) sc[(set * 32 + 16 * mt + 4 * fq + r) * 132 + 64 * kh + 16 * nj + fr] = d[r];
;       }
;   }
.LBB0_1652:
	v_lshlrev_b32_e32 v64, 2, v72
	v_mov_b32_e32 v66, v206
	v_and_b32_e32 v73, 7, v72
	v_and_b32_e32 v74, 0xffffffe0, v64
	v_lshlrev_b32_e32 v64, 9, v73
	v_and_or_b32 v84, v66, 15, v74
	v_and_b32_e32 v70, 0xffffff80, v66
	v_bfe_u32 v67, v66, 4, 2
	v_lshl_add_u64 v[68:69], s[58:59], 0, v[64:65]
	v_ashrrev_i32_e32 v71, 31, v70
	v_or_b32_e32 v90, 16, v84
	v_lshl_add_u64 v[68:69], v[70:71], 1, v[68:69]
	v_lshlrev_b32_e32 v64, 4, v67
	v_ashrrev_i32_e32 v85, 31, v84
	v_ashrrev_i32_e32 v91, 31, v90
	v_lshl_add_u64 v[88:89], v[68:69], 0, v[64:65]
	v_lshlrev_b64 v[68:69], 12, v[84:85]
	v_lshlrev_b64 v[90:91], 12, v[90:91]
	v_lshl_add_u64 v[116:117], v[88:89], 0, v[68:69]
	v_lshl_add_u64 v[120:121], v[88:89], 0, v[90:91]
	s_waitcnt vmcnt(0)
	v_mov_b32_e32 v68, v148
	v_mov_b32_e32 v69, v149
	v_mov_b32_e32 v70, v150
	v_mov_b32_e32 v71, v151
	v_mov_b32_e32 v76, v152
	v_mov_b32_e32 v77, v153
	v_mov_b32_e32 v78, v154
	v_mov_b32_e32 v79, v155
	v_mov_b32_e32 v92, v156
	v_mov_b32_e32 v93, v157
	v_mov_b32_e32 v94, v158
	v_mov_b32_e32 v95, v159
	v_mov_b32_e32 v96, v160
	v_mov_b32_e32 v97, v161
	v_mov_b32_e32 v98, v162
	v_mov_b32_e32 v99, v163
	v_ashrrev_i32_e32 v75, 2, v66
	v_and_b32_e32 v64, 0x4f, v66
	v_lshlrev_b32_e32 v64, 2, v64
	s_mov_b64 s[20:21], -1
	s_mov_b32 s69, 0
	v_mfma_f32_16x16x32_bf16 v[80:83], v[68:71], v[0:3], 0
	v_mfma_f32_16x16x32_bf16 v[84:87], v[68:71], v[56:59], 0
	v_mfma_f32_16x16x32_bf16 v[88:91], v[68:71], v[24:27], 0
	v_mfma_f32_16x16x32_bf16 v[68:71], v[68:71], v[44:47], 0
	v_mfma_f32_16x16x32_bf16 v[100:103], v[92:95], v[0:3], 0
	v_mfma_f32_16x16x32_bf16 v[104:107], v[92:95], v[56:59], 0
	v_mfma_f32_16x16x32_bf16 v[108:111], v[92:95], v[24:27], 0
	v_mfma_f32_16x16x32_bf16 v[80:83], v[76:79], v[4:7], v[80:83]
	v_mfma_f32_16x16x32_bf16 v[84:87], v[76:79], v[16:19], v[84:87]
	v_mfma_f32_16x16x32_bf16 v[88:91], v[76:79], v[28:31], v[88:91]
	v_mfma_f32_16x16x32_bf16 v[68:71], v[76:79], v[48:51], v[68:71]
	v_mfma_f32_16x16x32_bf16 v[76:79], v[96:99], v[4:7], v[100:103]
	v_mfma_f32_16x16x32_bf16 v[100:103], v[96:99], v[16:19], v[104:107]
	v_mfma_f32_16x16x32_bf16 v[104:107], v[96:99], v[28:31], v[108:111]
	s_nop 2
	s_nop 1
	v_mov_b32_e32 v108, v164
	v_mov_b32_e32 v109, v165
	v_mov_b32_e32 v110, v166
	v_mov_b32_e32 v111, v167
	v_mov_b32_e32 v112, v168
	v_mov_b32_e32 v113, v169
	v_mov_b32_e32 v114, v170
	v_mov_b32_e32 v115, v171
	v_mov_b32_e32 v116, v172
	v_mov_b32_e32 v117, v173
	v_mov_b32_e32 v118, v174
	v_mov_b32_e32 v119, v175
	s_nop 1
	v_mfma_f32_16x16x32_bf16 v[80:83], v[108:111], v[8:11], v[80:83]
	v_mfma_f32_16x16x32_bf16 v[84:87], v[108:111], v[20:23], v[84:87]
	v_mfma_f32_16x16x32_bf16 v[88:91], v[108:111], v[32:35], v[88:91]
	v_mfma_f32_16x16x32_bf16 v[68:71], v[108:111], v[52:55], v[68:71]
	s_nop 3
	v_mov_b32_e32 v108, v178
	v_mov_b32_e32 v109, v179
	v_mov_b32_e32 v110, v180
	v_mov_b32_e32 v111, v181
	v_add_u32_e32 v184, s90, v72
	v_min_u32_e32 v184, s68, v184
	v_lshrrev_b32_e32 v185, 3, v184
	v_lshlrev_b32_e32 v185, 17, v185
	v_and_b32_e32 v184, 7, v184
	v_lshl_or_b32 v184, v184, 9, v185
	v_mov_b32_e32 v185, 0
	v_lshl_add_u64 v[184:185], v[182:183], 0, v[184:185]
	v_mov_b32_e32 v186, 0x10000
	v_mov_b32_e32 v187, 0
	v_lshl_add_u64 v[186:187], v[184:185], 0, v[186:187]
	global_load_dwordx4 v[148:151], v[184:185], off
	global_load_dwordx4 v[152:155], v[184:185], off offset:64
	global_load_dwordx4 v[156:159], v[186:187], off
	global_load_dwordx4 v[160:163], v[186:187], off offset:64
	global_load_dwordx4 v[164:167], v[184:185], off offset:128
	global_load_dwordx4 v[168:171], v[184:185], off offset:192
	global_load_dwordx4 v[172:175], v[186:187], off offset:128
	global_load_dwordx4 v[178:181], v[186:187], off offset:192
	s_nop 1
	v_mfma_f32_16x16x32_bf16 v[80:83], v[112:115], v[12:15], v[80:83]
	v_mfma_f32_16x16x32_bf16 v[84:87], v[112:115], v[40:43], v[84:87]
	v_mfma_f32_16x16x32_bf16 v[88:91], v[112:115], v[36:39], v[88:91]
	v_mfma_f32_16x16x32_bf16 v[68:71], v[112:115], v[60:63], v[68:71]
	v_and_b32_e32 v112, 0xfffffe0, v75
	v_lshl_or_b32 v67, v67, 2, v112
	v_mul_lo_u32 v67, v67, s2
	v_add3_u32 v64, v146, v67, v64
	v_add_u32_e32 v67, 0x400, v64
	s_nop 0
	ds_write2_b32 v64, v80, v84 offset1:16
	ds_write2_b32 v64, v81, v85 offset0:132 offset1:148
	ds_write2_b32 v67, v82, v86 offset0:8 offset1:24
	ds_write2_b32 v67, v83, v87 offset0:140 offset1:156
	ds_write2_b32 v64, v88, v68 offset0:32 offset1:48
	v_mfma_f32_16x16x32_bf16 v[80:83], v[92:95], v[44:47], 0
	ds_write2_b32 v64, v89, v69 offset0:164 offset1:180
	ds_write2_b32 v67, v90, v70 offset0:40 offset1:56
	ds_write2_b32 v67, v91, v71 offset0:172 offset1:188
	v_add_u32_e32 v67, 0x2000, v64
	v_add_u32_e32 v64, 0x2400, v64
	v_mfma_f32_16x16x32_bf16 v[68:71], v[96:99], v[48:51], v[80:83]
	v_mfma_f32_16x16x32_bf16 v[76:79], v[116:119], v[8:11], v[76:79]
	v_mfma_f32_16x16x32_bf16 v[100:103], v[116:119], v[20:23], v[100:103]
	v_mfma_f32_16x16x32_bf16 v[104:107], v[116:119], v[32:35], v[104:107]
	v_mfma_f32_16x16x32_bf16 v[68:71], v[116:119], v[52:55], v[68:71]
	v_mfma_f32_16x16x32_bf16 v[76:79], v[108:111], v[12:15], v[76:79]
	v_mfma_f32_16x16x32_bf16 v[100:103], v[108:111], v[40:43], v[100:103]
	s_nop 7
	ds_write2_b32 v67, v76, v100 offset0:64 offset1:80
	ds_write2_b32 v67, v77, v101 offset0:196 offset1:212
	v_mfma_f32_16x16x32_bf16 v[104:107], v[108:111], v[36:39], v[104:107]
	ds_write2_b32 v64, v78, v102 offset0:72 offset1:88
	ds_write2_b32 v64, v79, v103 offset0:204 offset1:220
	v_mfma_f32_16x16x32_bf16 v[68:71], v[108:111], v[60:63], v[68:71]
	s_nop 7
	ds_write2_b32 v67, v104, v68 offset0:96 offset1:112
	ds_write2_b32 v67, v105, v69 offset0:228 offset1:244
	ds_write2_b32 v64, v106, v70 offset0:104 offset1:120
	ds_write2_b32 v64, v107, v71 offset0:236 offset1:252
	v_lshrrev_b32_e32 v236, 2, v66
	v_and_b32_e32 v237, 3, v66
	v_mul_u32_u24_e32 v238, 0x210, v236
	v_add_u32_e32 v238, v146, v238
	v_lshl_add_u32 v239, v237, 6, v238
	s_waitcnt lgkmcnt(0)
	s_barrier
; DI unsigned ordkey(float f) { const unsigned u = __float_as_uint(f); return (u & 0x80000000u) ? ~u : (u | 0x80000000u); }
; DI void peer_select_unit(const Params& p, int unit, char* lds, const bf16x8 (&kb)[4][4]) {
;     ...
;     const int rr = pass * 32 + (tid >> 3), part = tid & 7;
;     unsigned a[16], bq[16];
;     const float* srow = sc + rr * 132 + 16 * part;
; #pragma unroll
;     for (int j = 0; j < 4; ++j) {
;       const f32x4 v = *(const f32x4*)(srow + 4 * j);
; #pragma unroll
;       for (int e = 0; e < 4; ++e) a[4 * j + e] = (ordkey(v[e]) & ~127u) | (unsigned)(127 - (16 * part + 4 * j + e));
;     }
	ds_read_b128 v[124:127], v239 offset:0
	ds_read_b128 v[128:131], v239 offset:16
	ds_read_b128 v[132:135], v239 offset:32
	ds_read_b128 v[136:139], v239 offset:48
	ds_read_b128 v[212:215], v239 offset:256
	ds_read_b128 v[216:219], v239 offset:272
	ds_read_b128 v[220:223], v239 offset:288
	ds_read_b128 v[224:227], v239 offset:304
	v_lshlrev_b32_e32 v240, 4, v237
	v_sub_u32_e32 v241, 0x7f, v240
	v_sub_u32_e32 v242, 63, v240
	v_mov_b32_e32 v243, 0xffffff80
	v_bfrev_b32_e32 v240, 1
	s_waitcnt lgkmcnt(7)
	v_ashrrev_i32_e32 v122, 31, v124
	v_bitop3_b32 v124, v124, v122, v240 bitop3:0x1e
	v_and_or_b32 v124, v124, v243, v241
	v_ashrrev_i32_e32 v123, 31, v125
	v_bitop3_b32 v125, v125, v123, v240 bitop3:0x1e
	v_and_or_b32 v125, v125, v243, v241
	v_subrev_u32_e32 v125, 1, v125
	v_ashrrev_i32_e32 v140, 31, v126
	v_bitop3_b32 v126, v126, v140, v240 bitop3:0x1e
	v_and_or_b32 v126, v126, v243, v241
	v_subrev_u32_e32 v126, 2, v126
	v_ashrrev_i32_e32 v141, 31, v127
	v_bitop3_b32 v127, v127, v141, v240 bitop3:0x1e
	v_and_or_b32 v127, v127, v243, v241
	v_subrev_u32_e32 v127, 3, v127
	s_waitcnt lgkmcnt(6)
	v_ashrrev_i32_e32 v142, 31, v128
	v_bitop3_b32 v128, v128, v142, v240 bitop3:0x1e
	v_and_or_b32 v128, v128, v243, v241
	v_subrev_u32_e32 v128, 4, v128
	v_ashrrev_i32_e32 v143, 31, v129
	v_bitop3_b32 v129, v129, v143, v240 bitop3:0x1e
	v_and_or_b32 v129, v129, v243, v241
	v_subrev_u32_e32 v129, 5, v129
	v_ashrrev_i32_e32 v144, 31, v130
	v_bitop3_b32 v130, v130, v144, v240 bitop3:0x1e
	v_and_or_b32 v130, v130, v243, v241
	v_subrev_u32_e32 v130, 6, v130
	v_ashrrev_i32_e32 v145, 31, v131
	v_bitop3_b32 v131, v131, v145, v240 bitop3:0x1e
	v_and_or_b32 v131, v131, v243, v241
	v_subrev_u32_e32 v131, 7, v131
	s_waitcnt lgkmcnt(5)
	v_ashrrev_i32_e32 v194, 31, v132
	v_bitop3_b32 v132, v132, v194, v240 bitop3:0x1e
	v_and_or_b32 v132, v132, v243, v241
	v_subrev_u32_e32 v132, 8, v132
	v_ashrrev_i32_e32 v195, 31, v133
	v_bitop3_b32 v133, v133, v195, v240 bitop3:0x1e
	v_and_or_b32 v133, v133, v243, v241
	v_subrev_u32_e32 v133, 9, v133
	v_ashrrev_i32_e32 v196, 31, v134
	v_bitop3_b32 v134, v134, v196, v240 bitop3:0x1e
	v_and_or_b32 v134, v134, v243, v241
	v_subrev_u32_e32 v134, 10, v134
	v_ashrrev_i32_e32 v197, 31, v135
	v_bitop3_b32 v135, v135, v197, v240 bitop3:0x1e
	v_and_or_b32 v135, v135, v243, v241
	v_subrev_u32_e32 v135, 11, v135
	s_waitcnt lgkmcnt(4)
	v_ashrrev_i32_e32 v198, 31, v136
	v_bitop3_b32 v136, v136, v198, v240 bitop3:0x1e
	v_and_or_b32 v136, v136, v243, v241
	v_subrev_u32_e32 v136, 12, v136
	v_ashrrev_i32_e32 v199, 31, v137
	v_bitop3_b32 v137, v137, v199, v240 bitop3:0x1e
	v_and_or_b32 v137, v137, v243, v241
	v_subrev_u32_e32 v137, 13, v137
	v_ashrrev_i32_e32 v200, 31, v138
	v_bitop3_b32 v138, v138, v200, v240 bitop3:0x1e
	v_and_or_b32 v138, v138, v243, v241
	v_subrev_u32_e32 v138, 14, v138
	v_ashrrev_i32_e32 v201, 31, v139
	v_bitop3_b32 v139, v139, v201, v240 bitop3:0x1e
	v_and_or_b32 v139, v139, v243, v241
	v_subrev_u32_e32 v139, 15, v139
	s_waitcnt lgkmcnt(3)
	v_ashrrev_i32_e32 v202, 31, v212
	v_bitop3_b32 v212, v212, v202, v240 bitop3:0x1e
	v_and_or_b32 v212, v212, v243, v242
	v_ashrrev_i32_e32 v203, 31, v213
	v_bitop3_b32 v213, v213, v203, v240 bitop3:0x1e
	v_and_or_b32 v213, v213, v243, v242
	v_subrev_u32_e32 v213, 1, v213
	v_ashrrev_i32_e32 v204, 31, v214
	v_bitop3_b32 v214, v214, v204, v240 bitop3:0x1e
	v_and_or_b32 v214, v214, v243, v242
	v_subrev_u32_e32 v214, 2, v214
	v_ashrrev_i32_e32 v205, 31, v215
	v_bitop3_b32 v215, v215, v205, v240 bitop3:0x1e
	v_and_or_b32 v215, v215, v243, v242
	v_subrev_u32_e32 v215, 3, v215
	s_waitcnt lgkmcnt(2)
	v_ashrrev_i32_e32 v122, 31, v216
	v_bitop3_b32 v216, v216, v122, v240 bitop3:0x1e
	v_and_or_b32 v216, v216, v243, v242
	v_subrev_u32_e32 v216, 4, v216
	v_ashrrev_i32_e32 v123, 31, v217
	v_bitop3_b32 v217, v217, v123, v240 bitop3:0x1e
	v_and_or_b32 v217, v217, v243, v242
	v_subrev_u32_e32 v217, 5, v217
	v_ashrrev_i32_e32 v140, 31, v218
	v_bitop3_b32 v218, v218, v140, v240 bitop3:0x1e
	v_and_or_b32 v218, v218, v243, v242
	v_subrev_u32_e32 v218, 6, v218
	v_ashrrev_i32_e32 v141, 31, v219
	v_bitop3_b32 v219, v219, v141, v240 bitop3:0x1e
	v_and_or_b32 v219, v219, v243, v242
	v_subrev_u32_e32 v219, 7, v219
	s_waitcnt lgkmcnt(1)
	v_ashrrev_i32_e32 v142, 31, v220
	v_bitop3_b32 v220, v220, v142, v240 bitop3:0x1e
	v_and_or_b32 v220, v220, v243, v242
	v_subrev_u32_e32 v220, 8, v220
	v_ashrrev_i32_e32 v143, 31, v221
	v_bitop3_b32 v221, v221, v143, v240 bitop3:0x1e
	v_and_or_b32 v221, v221, v243, v242
	v_subrev_u32_e32 v221, 9, v221
	v_ashrrev_i32_e32 v144, 31, v222
	v_bitop3_b32 v222, v222, v144, v240 bitop3:0x1e
	v_and_or_b32 v222, v222, v243, v242
	v_subrev_u32_e32 v222, 10, v222
	v_ashrrev_i32_e32 v145, 31, v223
	v_bitop3_b32 v223, v223, v145, v240 bitop3:0x1e
	v_and_or_b32 v223, v223, v243, v242
	v_subrev_u32_e32 v223, 11, v223
	s_waitcnt lgkmcnt(0)
; DI unsigned ordkey(float f) { const unsigned u = __float_as_uint(f); return (u & 0x80000000u) ? ~u : (u | 0x80000000u); }
; #define CE_DESC(x, y) do { const unsigned mx_ = (x) > (y) ? (x) : (y); const unsigned mn_ = (x) > (y) ? (y) : (x); (x) = mx_; (y) = mn_; } while (0)
; DI void sort16_desc(unsigned (&a)[16]) {
; #pragma unroll
;   for (int k = 2; k <= 16; k <<= 1)
; #pragma unroll
;     for (int j = k >> 1; j > 0; j >>= 1)
; #pragma unroll
;       for (int i = 0; i < 16; ++i) {
;         const int l = i ^ j;
;         if (l > i) { if ((i & k) == 0) CE_DESC(a[i], a[l]); else CE_DESC(a[l], a[i]); }
;       }
; }
; DI void peer_select_unit(const Params& p, int unit, char* lds, const bf16x8 (&kb)[4][4]) {
;     ...
;     const float* srow = sc + rr * 132 + 16 * part;
; #pragma unroll
;     for (int j = 0; j < 4; ++j) {
;       const f32x4 v = *(const f32x4*)(srow + 4 * j);
; #pragma unroll
;       for (int e = 0; e < 4; ++e) a[4 * j + e] = (ordkey(v[e]) & ~127u) | (unsigned)(127 - (16 * part + 4 * j + e));
;     }
;     sort16_desc(a);
	v_ashrrev_i32_e32 v194, 31, v224
	v_bitop3_b32 v224, v224, v194, v240 bitop3:0x1e
	v_and_or_b32 v224, v224, v243, v242
	v_subrev_u32_e32 v224, 12, v224
	v_ashrrev_i32_e32 v195, 31, v225
	v_bitop3_b32 v225, v225, v195, v240 bitop3:0x1e
	v_and_or_b32 v225, v225, v243, v242
	v_subrev_u32_e32 v225, 13, v225
	v_ashrrev_i32_e32 v196, 31, v226
	v_bitop3_b32 v226, v226, v196, v240 bitop3:0x1e
	v_and_or_b32 v226, v226, v243, v242
	v_subrev_u32_e32 v226, 14, v226
	v_ashrrev_i32_e32 v197, 31, v227
	v_bitop3_b32 v227, v227, v197, v240 bitop3:0x1e
	v_and_or_b32 v227, v227, v243, v242
	v_subrev_u32_e32 v227, 15, v227
	v_max_u32_e32 v198, v124, v137
	v_min_u32_e32 v199, v124, v137
	v_max_u32_e32 v200, v212, v225
	v_min_u32_e32 v201, v212, v225
	v_max_u32_e32 v202, v125, v136
	v_min_u32_e32 v203, v125, v136
	v_max_u32_e32 v204, v213, v224
	v_min_u32_e32 v205, v213, v224
	v_max_u32_e32 v122, v126, v139
	v_min_u32_e32 v123, v126, v139
	v_max_u32_e32 v140, v214, v227
	v_min_u32_e32 v141, v214, v227
	v_max_u32_e32 v142, v127, v138
	v_min_u32_e32 v143, v127, v138
	v_max_u32_e32 v144, v215, v226
	v_min_u32_e32 v145, v215, v226
	v_max_u32_e32 v194, v128, v132
	v_min_u32_e32 v195, v128, v132
	v_max_u32_e32 v196, v216, v220
	v_min_u32_e32 v197, v216, v220
	v_max_u32_e32 v124, v129, v130
	v_min_u32_e32 v137, v129, v130
	v_max_u32_e32 v212, v217, v218
	v_min_u32_e32 v225, v217, v218
	v_max_u32_e32 v125, v131, v135
	v_min_u32_e32 v136, v131, v135
	v_max_u32_e32 v213, v219, v223
	v_min_u32_e32 v224, v219, v223
	v_max_u32_e32 v126, v133, v134
	v_min_u32_e32 v139, v133, v134
	v_max_u32_e32 v214, v221, v222
	v_min_u32_e32 v227, v221, v222
	v_max_u32_e32 v127, v198, v124
	v_min_u32_e32 v138, v198, v124
	v_max_u32_e32 v215, v200, v212
	v_min_u32_e32 v226, v200, v212
	v_max_u32_e32 v128, v202, v125
	v_min_u32_e32 v132, v202, v125
	v_max_u32_e32 v216, v204, v213
	v_min_u32_e32 v220, v204, v213
	v_max_u32_e32 v129, v122, v126
	v_min_u32_e32 v130, v122, v126
	v_max_u32_e32 v217, v140, v214
	v_min_u32_e32 v218, v140, v214
	v_max_u32_e32 v131, v142, v194
	v_min_u32_e32 v135, v142, v194
	v_max_u32_e32 v219, v144, v196
	v_min_u32_e32 v223, v144, v196
	v_max_u32_e32 v133, v137, v199
	v_min_u32_e32 v134, v137, v199
	v_max_u32_e32 v221, v225, v201
	v_min_u32_e32 v222, v225, v201
	v_max_u32_e32 v198, v195, v143
	v_min_u32_e32 v124, v195, v143
	v_max_u32_e32 v200, v197, v145
	v_min_u32_e32 v212, v197, v145
	v_max_u32_e32 v202, v139, v123
	v_min_u32_e32 v125, v139, v123
	v_max_u32_e32 v204, v227, v141
	v_min_u32_e32 v213, v227, v141
	v_max_u32_e32 v122, v136, v203
	v_min_u32_e32 v126, v136, v203
	v_max_u32_e32 v140, v224, v205
	v_min_u32_e32 v214, v224, v205
	v_max_u32_e32 v142, v127, v128
	v_min_u32_e32 v194, v127, v128
	v_max_u32_e32 v144, v215, v216
	v_min_u32_e32 v196, v215, v216
	v_max_u32_e32 v137, v129, v131
	v_min_u32_e32 v199, v129, v131
	v_max_u32_e32 v225, v217, v219
	v_min_u32_e32 v201, v217, v219
	v_max_u32_e32 v195, v135, v138
	v_min_u32_e32 v143, v135, v138
	v_max_u32_e32 v197, v223, v226
	v_min_u32_e32 v145, v223, v226
	v_max_u32_e32 v139, v133, v198
	v_min_u32_e32 v123, v133, v198
	v_max_u32_e32 v227, v221, v200
	v_min_u32_e32 v141, v221, v200
	v_max_u32_e32 v136, v132, v130
	v_min_u32_e32 v203, v132, v130
	v_max_u32_e32 v224, v220, v218
	v_min_u32_e32 v205, v220, v218
	v_max_u32_e32 v127, v202, v122
	v_min_u32_e32 v128, v202, v122
	v_max_u32_e32 v215, v204, v140
	v_min_u32_e32 v216, v204, v140
	v_max_u32_e32 v129, v126, v134
	v_min_u32_e32 v131, v126, v134
	v_max_u32_e32 v217, v214, v222
	v_min_u32_e32 v219, v214, v222
	v_max_u32_e32 v135, v124, v125
	v_min_u32_e32 v138, v124, v125
	v_max_u32_e32 v223, v212, v213
	v_min_u32_e32 v226, v212, v213
	v_max_u32_e32 v133, v142, v137
	v_min_u32_e32 v198, v142, v137
	v_max_u32_e32 v221, v144, v225
	v_min_u32_e32 v200, v144, v225
	v_max_u32_e32 v132, v194, v199
	v_min_u32_e32 v130, v194, v199
	v_max_u32_e32 v220, v196, v201
	v_min_u32_e32 v218, v196, v201
	v_max_u32_e32 v202, v195, v127
	v_min_u32_e32 v122, v195, v127
	v_max_u32_e32 v204, v197, v215
	v_min_u32_e32 v140, v197, v215
	v_max_u32_e32 v126, v143, v128
	v_min_u32_e32 v134, v143, v128
	v_max_u32_e32 v214, v145, v216
	v_min_u32_e32 v222, v145, v216
	v_max_u32_e32 v124, v139, v136
	v_min_u32_e32 v125, v139, v136
	v_max_u32_e32 v212, v227, v224
	v_min_u32_e32 v213, v227, v224
	v_max_u32_e32 v142, v123, v203
	v_min_u32_e32 v137, v123, v203
	v_max_u32_e32 v144, v141, v205
	v_min_u32_e32 v225, v141, v205
	v_max_u32_e32 v194, v129, v135
	v_min_u32_e32 v199, v129, v135
	v_max_u32_e32 v196, v217, v223
	v_min_u32_e32 v201, v217, v223
	v_max_u32_e32 v195, v131, v138
	v_min_u32_e32 v127, v131, v138
	v_max_u32_e32 v197, v219, v226
	v_min_u32_e32 v215, v219, v226
	v_max_u32_e32 v143, v132, v198
	v_min_u32_e32 v128, v132, v198
	v_max_u32_e32 v145, v220, v200
	v_min_u32_e32 v216, v220, v200
	v_max_u32_e32 v139, v130, v194
	v_min_u32_e32 v136, v130, v194
	v_max_u32_e32 v227, v218, v196
	v_min_u32_e32 v224, v218, v196
	v_max_u32_e32 v123, v202, v124
	v_min_u32_e32 v203, v202, v124
	v_max_u32_e32 v141, v204, v212
	v_min_u32_e32 v205, v204, v212
	v_max_u32_e32 v129, v126, v125
	v_min_u32_e32 v135, v126, v125
	v_max_u32_e32 v217, v214, v213
	v_min_u32_e32 v223, v214, v213
	v_max_u32_e32 v131, v142, v122
	v_min_u32_e32 v138, v142, v122
	v_max_u32_e32 v219, v144, v140
	v_min_u32_e32 v226, v144, v140
	v_max_u32_e32 v132, v137, v134
	v_min_u32_e32 v198, v137, v134
	v_max_u32_e32 v220, v225, v222
	v_min_u32_e32 v200, v225, v222
	v_max_u32_e32 v130, v195, v199
	v_min_u32_e32 v194, v195, v199
	v_max_u32_e32 v218, v197, v201
	v_min_u32_e32 v196, v197, v201
	v_max_u32_e32 v202, v143, v123
; #define CE_DESC(x, y) do { const unsigned mx_ = (x) > (y) ? (x) : (y); const unsigned mn_ = (x) > (y) ? (y) : (x); (x) = mx_; (y) = mn_; } while (0)
; DI void sort16_desc(unsigned (&a)[16]) {
; #pragma unroll
;   for (int k = 2; k <= 16; k <<= 1)
; #pragma unroll
;     for (int j = k >> 1; j > 0; j >>= 1)
; #pragma unroll
;       for (int i = 0; i < 16; ++i) {
;         const int l = i ^ j;
;         if (l > i) { if ((i & k) == 0) CE_DESC(a[i], a[l]); else CE_DESC(a[l], a[i]); }
;       }
; }
; DI void merge16_desc(unsigned (&a)[16], const unsigned (&b)[16]) {
; #pragma unroll
;   for (int i = 0; i < 16; ++i) a[i] = a[i] > b[15 - i] ? a[i] : b[15 - i];
; #pragma unroll
;   for (int j = 8; j > 0; j >>= 1)
; #pragma unroll
;     for (int i = 0; i < 16; ++i) if ((i & j) == 0) CE_DESC(a[i], a[i + j]);
; }
; DI void peer_select_unit(const Params& p, int unit, char* lds, const bf16x8 (&kb)[4][4]) {
;     ...
;     dpp16<0xB1>(bq, a); merge16_desc(a, bq);
	v_min_u32_e32 v124, v143, v123
	v_max_u32_e32 v204, v145, v141
	v_min_u32_e32 v212, v145, v141
	v_max_u32_e32 v126, v128, v203
	v_min_u32_e32 v125, v128, v203
	v_max_u32_e32 v214, v216, v205
	v_min_u32_e32 v213, v216, v205
	v_max_u32_e32 v142, v129, v131
	v_min_u32_e32 v122, v129, v131
	v_max_u32_e32 v144, v217, v219
	v_min_u32_e32 v140, v217, v219
	v_max_u32_e32 v137, v135, v138
	v_min_u32_e32 v134, v135, v138
	v_max_u32_e32 v225, v223, v226
	v_min_u32_e32 v222, v223, v226
	v_max_u32_e32 v195, v132, v130
	v_min_u32_e32 v199, v132, v130
	v_max_u32_e32 v197, v220, v218
	v_min_u32_e32 v201, v220, v218
	v_max_u32_e32 v143, v198, v194
	v_min_u32_e32 v123, v198, v194
	v_max_u32_e32 v145, v200, v196
	v_min_u32_e32 v141, v200, v196
	v_max_u32_e32 v128, v126, v124
	v_min_u32_e32 v203, v126, v124
	v_max_u32_e32 v216, v214, v212
	v_min_u32_e32 v205, v214, v212
	v_max_u32_e32 v129, v139, v125
	v_min_u32_e32 v131, v139, v125
	v_max_u32_e32 v217, v227, v213
	v_min_u32_e32 v219, v227, v213
	v_max_u32_e32 v135, v195, v136
	v_min_u32_e32 v138, v195, v136
	v_max_u32_e32 v223, v197, v224
	v_min_u32_e32 v226, v197, v224
	v_max_u32_e32 v132, v143, v199
	v_min_u32_e32 v130, v143, v199
	v_max_u32_e32 v220, v145, v201
	v_min_u32_e32 v218, v145, v201
	v_max_u32_e32 v198, v129, v142
	v_min_u32_e32 v194, v129, v142
	v_max_u32_e32 v200, v217, v144
	v_min_u32_e32 v196, v217, v144
	v_max_u32_e32 v126, v131, v122
	v_min_u32_e32 v124, v131, v122
	v_max_u32_e32 v214, v219, v140
	v_min_u32_e32 v212, v219, v140
	v_max_u32_e32 v139, v137, v135
	v_min_u32_e32 v125, v137, v135
	v_max_u32_e32 v227, v225, v223
	v_min_u32_e32 v213, v225, v223
	v_max_u32_e32 v195, v134, v138
	v_min_u32_e32 v136, v134, v138
	v_max_u32_e32 v197, v222, v226
	v_min_u32_e32 v224, v222, v226
	v_max_u32_e32 v143, v198, v203
	v_min_u32_e32 v199, v198, v203
	v_max_u32_e32 v145, v200, v205
	v_min_u32_e32 v201, v200, v205
	v_max_u32_e32 v129, v194, v126
	v_min_u32_e32 v142, v194, v126
	v_max_u32_e32 v217, v196, v214
	v_min_u32_e32 v144, v196, v214
	v_max_u32_e32 v131, v139, v124
	v_min_u32_e32 v122, v139, v124
	v_max_u32_e32 v219, v227, v212
	v_min_u32_e32 v140, v227, v212
	v_max_u32_e32 v137, v125, v195
	v_min_u32_e32 v135, v125, v195
	v_max_u32_e32 v225, v213, v197
	v_min_u32_e32 v223, v213, v197
	v_max_u32_e32 v134, v132, v136
	v_min_u32_e32 v138, v132, v136
	v_max_u32_e32 v222, v220, v224
	v_min_u32_e32 v226, v220, v224
	v_max_u32_e32 v198, v142, v131
	v_min_u32_e32 v203, v142, v131
	v_max_u32_e32 v200, v144, v219
	v_min_u32_e32 v205, v144, v219
	v_max_u32_e32 v194, v122, v137
	v_min_u32_e32 v126, v122, v137
	v_max_u32_e32 v196, v140, v225
	v_min_u32_e32 v214, v140, v225
	v_max_u32_e32 v139, v133, v215
	v_max_u32_e32 v124, v202, v141
	v_max_u32_e32 v227, v128, v218
	v_max_u32_e32 v212, v143, v226
	v_max_u32_e32 v125, v199, v222
	v_max_u32_e32 v195, v129, v223
	v_max_u32_e32 v213, v198, v214
	v_max_u32_e32 v197, v203, v196
	v_max_u32_e32 v132, v194, v205
	v_max_u32_e32 v136, v126, v200
	v_max_u32_e32 v220, v135, v217
	v_max_u32_e32 v224, v134, v201
	v_max_u32_e32 v142, v138, v145
	v_max_u32_e32 v131, v130, v216
	v_max_u32_e32 v144, v123, v204
	v_max_u32_e32 v219, v127, v221
	v_max_u32_e32 v122, v139, v132
	v_min_u32_e32 v137, v139, v132
	v_max_u32_e32 v140, v124, v136
	v_min_u32_e32 v225, v124, v136
	v_max_u32_e32 v133, v227, v220
	v_min_u32_e32 v202, v227, v220
	v_max_u32_e32 v128, v212, v224
	v_min_u32_e32 v143, v212, v224
	v_max_u32_e32 v199, v125, v142
	v_min_u32_e32 v129, v125, v142
	v_max_u32_e32 v198, v195, v131
	v_min_u32_e32 v203, v195, v131
	v_max_u32_e32 v194, v213, v144
	v_min_u32_e32 v126, v213, v144
	v_max_u32_e32 v135, v197, v219
	v_min_u32_e32 v134, v197, v219
	v_max_u32_e32 v138, v122, v199
	v_min_u32_e32 v130, v122, v199
	v_max_u32_e32 v123, v140, v198
	v_min_u32_e32 v127, v140, v198
	v_max_u32_e32 v221, v133, v194
	v_min_u32_e32 v204, v133, v194
	v_max_u32_e32 v216, v128, v135
	v_min_u32_e32 v145, v128, v135
	v_max_u32_e32 v201, v137, v129
	v_min_u32_e32 v217, v137, v129
	v_max_u32_e32 v200, v225, v203
	v_min_u32_e32 v205, v225, v203
	v_max_u32_e32 v196, v202, v126
	v_min_u32_e32 v214, v202, v126
	v_max_u32_e32 v223, v143, v134
	v_min_u32_e32 v222, v143, v134
	v_max_u32_e32 v226, v138, v221
	v_min_u32_e32 v218, v138, v221
	v_max_u32_e32 v141, v123, v216
	v_min_u32_e32 v215, v123, v216
	v_max_u32_e32 v139, v130, v204
	v_min_u32_e32 v132, v130, v204
	v_max_u32_e32 v124, v127, v145
	v_min_u32_e32 v136, v127, v145
	v_max_u32_e32 v227, v201, v196
	v_min_u32_e32 v220, v201, v196
	v_max_u32_e32 v212, v200, v223
	v_min_u32_e32 v224, v200, v223
	v_max_u32_e32 v125, v217, v214
	v_min_u32_e32 v142, v217, v214
	v_max_u32_e32 v195, v205, v222
	v_min_u32_e32 v131, v205, v222
	v_max_u32_e32 v213, v226, v141
	v_min_u32_e32 v144, v226, v141
	v_max_u32_e32 v197, v218, v215
	v_min_u32_e32 v219, v218, v215
	v_max_u32_e32 v122, v139, v124
	v_min_u32_e32 v199, v139, v124
	v_max_u32_e32 v140, v132, v136
	v_min_u32_e32 v198, v132, v136
	v_max_u32_e32 v133, v227, v212
	v_min_u32_e32 v194, v227, v212
	v_max_u32_e32 v128, v220, v224
	v_min_u32_e32 v135, v220, v224
	v_max_u32_e32 v137, v125, v195
	v_min_u32_e32 v129, v125, v195
	v_max_u32_e32 v225, v142, v131
	v_min_u32_e32 v203, v142, v131
	s_nop 1
	v_max_u32_dpp v202, v203, v213 quad_perm:[1,0,3,2] row_mask:0xf bank_mask:0xf
	v_max_u32_dpp v126, v225, v144 quad_perm:[1,0,3,2] row_mask:0xf bank_mask:0xf
	v_max_u32_dpp v143, v129, v197 quad_perm:[1,0,3,2] row_mask:0xf bank_mask:0xf
	v_max_u32_dpp v134, v137, v219 quad_perm:[1,0,3,2] row_mask:0xf bank_mask:0xf
	v_max_u32_dpp v138, v135, v122 quad_perm:[1,0,3,2] row_mask:0xf bank_mask:0xf
; #define CE_DESC(x, y) do { const unsigned mx_ = (x) > (y) ? (x) : (y); const unsigned mn_ = (x) > (y) ? (y) : (x); (x) = mx_; (y) = mn_; } while (0)
; DI void merge16_desc(unsigned (&a)[16], const unsigned (&b)[16]) {
; #pragma unroll
;   for (int i = 0; i < 16; ++i) a[i] = a[i] > b[15 - i] ? a[i] : b[15 - i];
; #pragma unroll
;   for (int j = 8; j > 0; j >>= 1)
; #pragma unroll
;     for (int i = 0; i < 16; ++i) if ((i & j) == 0) CE_DESC(a[i], a[i + j]);
; }
; template <int CTRL> DI void dpp16(unsigned (&b)[16], const unsigned (&a)[16]) {
; #pragma unroll
;   for (int s = 0; s < 16; ++s) b[s] = (unsigned)__builtin_amdgcn_update_dpp(0, (int)a[s], CTRL, 0xF, 0xF, true);
; DI void peer_select_unit(const Params& p, int unit, char* lds, const bf16x8 (&kb)[4][4]) {
;     ...
;     dpp16<0xB1>(bq, a); merge16_desc(a, bq);
;     dpp16<0x4E>(bq, a); merge16_desc(a, bq);
	v_max_u32_dpp v221, v128, v199 quad_perm:[1,0,3,2] row_mask:0xf bank_mask:0xf
	v_max_u32_dpp v123, v194, v140 quad_perm:[1,0,3,2] row_mask:0xf bank_mask:0xf
	v_max_u32_dpp v216, v133, v198 quad_perm:[1,0,3,2] row_mask:0xf bank_mask:0xf
	v_max_u32_dpp v130, v198, v133 quad_perm:[1,0,3,2] row_mask:0xf bank_mask:0xf
	v_max_u32_dpp v204, v140, v194 quad_perm:[1,0,3,2] row_mask:0xf bank_mask:0xf
	v_max_u32_dpp v127, v199, v128 quad_perm:[1,0,3,2] row_mask:0xf bank_mask:0xf
	v_max_u32_dpp v145, v122, v135 quad_perm:[1,0,3,2] row_mask:0xf bank_mask:0xf
	v_max_u32_dpp v201, v219, v137 quad_perm:[1,0,3,2] row_mask:0xf bank_mask:0xf
	v_max_u32_dpp v196, v197, v129 quad_perm:[1,0,3,2] row_mask:0xf bank_mask:0xf
	v_max_u32_dpp v200, v144, v225 quad_perm:[1,0,3,2] row_mask:0xf bank_mask:0xf
	v_max_u32_dpp v223, v213, v203 quad_perm:[1,0,3,2] row_mask:0xf bank_mask:0xf
	v_max_u32_e32 v217, v202, v130
	v_min_u32_e32 v214, v202, v130
	v_max_u32_e32 v205, v126, v204
	v_min_u32_e32 v222, v126, v204
	v_max_u32_e32 v226, v143, v127
	v_min_u32_e32 v141, v143, v127
	v_max_u32_e32 v218, v134, v145
	v_min_u32_e32 v215, v134, v145
	v_max_u32_e32 v139, v138, v201
	v_min_u32_e32 v124, v138, v201
	v_max_u32_e32 v132, v221, v196
	v_min_u32_e32 v136, v221, v196
	v_max_u32_e32 v227, v123, v200
	v_min_u32_e32 v212, v123, v200
	v_max_u32_e32 v220, v216, v223
	v_min_u32_e32 v224, v216, v223
	v_max_u32_e32 v125, v217, v139
	v_min_u32_e32 v195, v217, v139
	v_max_u32_e32 v142, v205, v132
	v_min_u32_e32 v131, v205, v132
	v_max_u32_e32 v213, v226, v227
	v_min_u32_e32 v144, v226, v227
	v_max_u32_e32 v197, v218, v220
	v_min_u32_e32 v219, v218, v220
	v_max_u32_e32 v122, v214, v124
	v_min_u32_e32 v199, v214, v124
	v_max_u32_e32 v140, v222, v136
	v_min_u32_e32 v198, v222, v136
	v_max_u32_e32 v133, v141, v212
	v_min_u32_e32 v194, v141, v212
	v_max_u32_e32 v128, v215, v224
	v_min_u32_e32 v135, v215, v224
	v_max_u32_e32 v137, v125, v213
	v_min_u32_e32 v129, v125, v213
	v_max_u32_e32 v225, v142, v197
	v_min_u32_e32 v203, v142, v197
	v_max_u32_e32 v202, v195, v144
	v_min_u32_e32 v130, v195, v144
	v_max_u32_e32 v126, v131, v219
	v_min_u32_e32 v204, v131, v219
	v_max_u32_e32 v143, v122, v133
	v_min_u32_e32 v127, v122, v133
	v_max_u32_e32 v134, v140, v128
	v_min_u32_e32 v145, v140, v128
	v_max_u32_e32 v138, v199, v194
	v_min_u32_e32 v201, v199, v194
	v_max_u32_e32 v221, v198, v135
	v_min_u32_e32 v196, v198, v135
	v_max_u32_e32 v123, v137, v225
	v_min_u32_e32 v200, v137, v225
	v_max_u32_e32 v216, v129, v203
	v_min_u32_e32 v223, v129, v203
	v_max_u32_e32 v217, v202, v126
	v_min_u32_e32 v139, v202, v126
	v_max_u32_e32 v205, v130, v204
	v_min_u32_e32 v132, v130, v204
	v_max_u32_e32 v226, v143, v134
	v_min_u32_e32 v227, v143, v134
	v_max_u32_e32 v218, v127, v145
	v_min_u32_e32 v220, v127, v145
	v_max_u32_e32 v214, v138, v221
	v_min_u32_e32 v124, v138, v221
	v_max_u32_e32 v222, v201, v196
	v_min_u32_e32 v136, v201, v196
	s_nop 1
	v_max_u32_dpp v141, v136, v123 quad_perm:[2,3,0,1] row_mask:0xf bank_mask:0xf
	v_max_u32_dpp v212, v222, v200 quad_perm:[2,3,0,1] row_mask:0xf bank_mask:0xf
	v_max_u32_dpp v215, v124, v216 quad_perm:[2,3,0,1] row_mask:0xf bank_mask:0xf
	v_max_u32_dpp v224, v214, v223 quad_perm:[2,3,0,1] row_mask:0xf bank_mask:0xf
	v_max_u32_dpp v125, v220, v217 quad_perm:[2,3,0,1] row_mask:0xf bank_mask:0xf
	v_max_u32_dpp v213, v218, v139 quad_perm:[2,3,0,1] row_mask:0xf bank_mask:0xf
	v_max_u32_dpp v142, v227, v205 quad_perm:[2,3,0,1] row_mask:0xf bank_mask:0xf
	v_max_u32_dpp v197, v226, v132 quad_perm:[2,3,0,1] row_mask:0xf bank_mask:0xf
	v_max_u32_dpp v195, v132, v226 quad_perm:[2,3,0,1] row_mask:0xf bank_mask:0xf
	v_max_u32_dpp v144, v205, v227 quad_perm:[2,3,0,1] row_mask:0xf bank_mask:0xf
	v_max_u32_dpp v131, v139, v218 quad_perm:[2,3,0,1] row_mask:0xf bank_mask:0xf
	v_max_u32_dpp v219, v217, v220 quad_perm:[2,3,0,1] row_mask:0xf bank_mask:0xf
	v_max_u32_dpp v122, v223, v214 quad_perm:[2,3,0,1] row_mask:0xf bank_mask:0xf
	v_max_u32_dpp v133, v216, v124 quad_perm:[2,3,0,1] row_mask:0xf bank_mask:0xf
	v_max_u32_dpp v140, v200, v222 quad_perm:[2,3,0,1] row_mask:0xf bank_mask:0xf
	v_max_u32_dpp v128, v123, v136 quad_perm:[2,3,0,1] row_mask:0xf bank_mask:0xf
	v_max_u32_e32 v199, v141, v195
	v_min_u32_e32 v194, v141, v195
	v_max_u32_e32 v198, v212, v144
	v_min_u32_e32 v135, v212, v144
	v_max_u32_e32 v137, v215, v131
	v_min_u32_e32 v225, v215, v131
	v_max_u32_e32 v129, v224, v219
	v_min_u32_e32 v203, v224, v219
	v_max_u32_e32 v202, v125, v122
	v_min_u32_e32 v126, v125, v122
	v_max_u32_e32 v130, v213, v133
	v_min_u32_e32 v204, v213, v133
	v_max_u32_e32 v143, v142, v140
	v_min_u32_e32 v134, v142, v140
	v_max_u32_e32 v127, v197, v128
	v_min_u32_e32 v145, v197, v128
	v_max_u32_e32 v138, v199, v202
	v_min_u32_e32 v221, v199, v202
	v_max_u32_e32 v201, v198, v130
	v_min_u32_e32 v196, v198, v130
	v_max_u32_e32 v123, v137, v143
	v_min_u32_e32 v200, v137, v143
	v_max_u32_e32 v216, v129, v127
	v_min_u32_e32 v223, v129, v127
	v_max_u32_e32 v217, v194, v126
	v_min_u32_e32 v139, v194, v126
	v_max_u32_e32 v205, v135, v204
	v_min_u32_e32 v132, v135, v204
	v_max_u32_e32 v226, v225, v134
	v_min_u32_e32 v227, v225, v134
	v_max_u32_e32 v218, v203, v145
	v_min_u32_e32 v220, v203, v145
	v_max_u32_e32 v214, v138, v123
	v_min_u32_e32 v124, v138, v123
	v_max_u32_e32 v222, v201, v216
	v_min_u32_e32 v136, v201, v216
	v_max_u32_e32 v141, v221, v200
	v_min_u32_e32 v195, v221, v200
	v_max_u32_e32 v212, v196, v223
	v_min_u32_e32 v144, v196, v223
	v_max_u32_e32 v215, v217, v226
	v_min_u32_e32 v131, v217, v226
	v_max_u32_e32 v224, v205, v218
	v_min_u32_e32 v219, v205, v218
	v_max_u32_e32 v125, v139, v227
; DI unsigned ordkey(float f) { const unsigned u = __float_as_uint(f); return (u & 0x80000000u) ? ~u : (u | 0x80000000u); }
; DI void peer_select_unit(const Params& p, int unit, char* lds, const bf16x8 (&kb)[4][4]) {
;     ...
; #pragma unroll
;     for (int s = 0; s < 2; ++s) {
;       unsigned k = 0u;
; #pragma unroll
;       for (int q = 0; q < 8; ++q) k = part == q ? a[2 * q + s] : k;
;       const int idx = 127 - (int)(k & 127u);
;       topv[rr * 16 + 2 * part + s] = sc[rr * 132 + idx]; topi[rr * 16 + 2 * part + s] = idx;
;     }
;   }
;     ...
;   if (tid < 128) {
;     const int tok = tid >> 2, q4 = tid & 3;
;     unsigned c[16], bq[16];
; #pragma unroll
;     for (int i = 0; i < 16; ++i) {
;       const unsigned code = PEER_CAND[16 * q4 + i];
;       const float v = topv[tok * 16 + ((code >> 4) & 15)] + topv[(32 + tok) * 16 + (code & 15)];
;       c[i] = code == 0xFFu ? 0u : ((ordkey(v) & ~255u) | (255u - code));
;     }
	v_min_u32_e32 v122, v139, v227
	v_max_u32_e32 v213, v132, v220
	v_min_u32_e32 v133, v132, v220
	v_max_u32_e32 v142, v214, v222
	v_min_u32_e32 v140, v214, v222
	v_max_u32_e32 v197, v124, v136
	v_min_u32_e32 v128, v124, v136
	v_max_u32_e32 v199, v141, v212
	v_min_u32_e32 v202, v141, v212
	v_max_u32_e32 v198, v195, v144
	v_min_u32_e32 v130, v195, v144
	v_max_u32_e32 v137, v215, v224
	v_min_u32_e32 v143, v215, v224
	v_max_u32_e32 v129, v131, v219
	v_min_u32_e32 v127, v131, v219
	v_max_u32_e32 v194, v125, v213
	v_min_u32_e32 v126, v125, v213
	v_max_u32_e32 v135, v122, v133
	v_min_u32_e32 v204, v122, v133
	v_cmp_eq_u32_e32 vcc, 1, v237
	s_nop 1
	v_cndmask_b32_e32 v225, v142, v199, vcc
	v_cndmask_b32_e32 v134, v140, v202, vcc
	v_cndmask_b32_e32 v203, v197, v198, vcc
	v_cndmask_b32_e32 v145, v128, v130, vcc
	v_cmp_eq_u32_e32 vcc, 2, v237
	s_nop 1
	v_cndmask_b32_e32 v225, v225, v137, vcc
	v_cndmask_b32_e32 v134, v134, v143, vcc
	v_cndmask_b32_e32 v203, v203, v129, vcc
	v_cndmask_b32_e32 v145, v145, v127, vcc
	v_cmp_eq_u32_e32 vcc, 3, v237
	s_nop 1
	v_cndmask_b32_e32 v225, v225, v194, vcc
	v_cndmask_b32_e32 v134, v134, v126, vcc
	v_cndmask_b32_e32 v203, v203, v135, vcc
	v_cndmask_b32_e32 v145, v145, v204, vcc
	v_and_b32_e32 v240, 0x7f, v225
	v_sub_u32_e32 v228, 0x7f, v240
	v_lshl_add_u32 v225, v228, 2, v238
	ds_read_b32 v232, v225
	v_and_b32_e32 v240, 0x7f, v134
	v_sub_u32_e32 v229, 0x7f, v240
	v_lshl_add_u32 v134, v229, 2, v238
	ds_read_b32 v233, v134
	v_and_b32_e32 v240, 0x7f, v203
	v_sub_u32_e32 v230, 0x7f, v240
	v_lshl_add_u32 v203, v230, 2, v238
	ds_read_b32 v234, v203
	v_and_b32_e32 v240, 0x7f, v145
	v_sub_u32_e32 v231, 0x7f, v240
	v_lshl_add_u32 v145, v231, 2, v238
	ds_read_b32 v235, v145
	v_lshlrev_b32_e32 v239, 6, v236
	v_lshl_add_u32 v239, v237, 4, v239
	v_add_u32_e32 v239, v146, v239
	ds_write_b128 v239, v[228:231] offset:37888
	s_waitcnt lgkmcnt(1)
	ds_write_b128 v239, v[232:235] offset:33792
	v_xor_b32_e32 v66, v249, v66
	v_cmp_gt_i32_e32 vcc, s18, v66
	s_waitcnt lgkmcnt(0)
	s_barrier
	s_and_saveexec_b64 s[8:9], vcc
	s_cbranch_execz .LBB0_1651
	v_and_b32_e32 v77, 3, v66
	v_lshrrev_b32_e32 v75, 2, v66
	v_lshlrev_b32_e32 v64, 4, v77
	v_and_b32_e32 v80, 0xffff, v244
	v_lshlrev_b32_e32 v66, 6, v75
	v_lshlrev_b32_e32 v76, 4, v75
	v_cmp_eq_u32_e32 vcc, 3, v77
	v_cmp_ne_u32_e64 s[0:1], 3, v77
	v_mov_b32_e32 v82, 0
	v_lshrrev_b32_e32 v67, 2, v80
	v_and_b32_e32 v68, 15, v80
	v_lshrrev_b16_e32 v79, 8, v80
	v_and_b32_e32 v67, 60, v67
	v_lshlrev_b32_e32 v68, 2, v68
	v_lshrrev_b32_e32 v69, 2, v79
	v_and_b32_e32 v78, 15, v79
	v_add3_u32 v67, v146, v67, v66
	v_add3_u32 v68, v146, v68, v66
	v_and_b32_e32 v69, 60, v69
	v_lshlrev_b32_e32 v78, 2, v78
	v_add3_u32 v81, v146, v69, v66
	v_add3_u32 v78, v146, v78, v66
	ds_read_b32 v67, v67 offset:33792
	ds_read_b32 v69, v68 offset:35840
	ds_read_b32 v66, v81 offset:33792
	ds_read_b32 v68, v78 offset:35840
	v_mov_b32_e32 v81, 0
	v_lshlrev_b32_e32 v78, 2, v76
	v_mov_b32_e32 v83, 0
	v_mov_b32_e32 v84, 0
	v_mov_b32_e32 v85, 0
	v_mov_b32_e32 v86, 0
	v_mov_b32_e32 v87, 0
	v_mov_b32_e32 v88, 0
	v_mov_b32_e32 v89, 0
	v_mov_b32_e32 v90, 0
	v_mov_b32_e32 v91, 0
	v_mov_b32_e32 v92, 0
	v_mov_b32_e32 v93, 0
	v_mov_b32_e32 v94, 0
	s_and_saveexec_b64 s[6:7], s[0:1]
	v_bfe_u32 v82, v244, 16, 8
	v_lshrrev_b32_e32 v238, 2, v82
	v_and_b32_e32 v239, 15, v82
	v_and_b32_e32 v238, 60, v238
	v_lshlrev_b32_e32 v239, 2, v239
	v_add3_u32 v238, v146, v238, v78
	v_add3_u32 v239, v146, v239, v78
	ds_read_b32 v210, v238 offset:33792
	ds_read_b32 v211, v239 offset:35840
	v_bfe_u32 v81, v244, 24, 8
	v_lshrrev_b32_e32 v238, 2, v81
	v_and_b32_e32 v239, 15, v81
	v_and_b32_e32 v238, 60, v238
	v_lshlrev_b32_e32 v239, 2, v239
	v_add3_u32 v238, v146, v238, v78
	v_add3_u32 v239, v146, v239, v78
	ds_read_b32 v212, v238 offset:33792
	ds_read_b32 v213, v239 offset:35840
	v_bfe_u32 v84, v245, 0, 8
	v_lshrrev_b32_e32 v238, 2, v84
	v_and_b32_e32 v239, 15, v84
	v_and_b32_e32 v238, 60, v238
	v_lshlrev_b32_e32 v239, 2, v239
	v_add3_u32 v238, v146, v238, v78
	v_add3_u32 v239, v146, v239, v78
	ds_read_b32 v214, v238 offset:33792
	ds_read_b32 v215, v239 offset:35840
	v_bfe_u32 v83, v245, 8, 8
	v_lshrrev_b32_e32 v238, 2, v83
	v_and_b32_e32 v239, 15, v83
	v_and_b32_e32 v238, 60, v238
	v_lshlrev_b32_e32 v239, 2, v239
	v_add3_u32 v238, v146, v238, v78
	v_add3_u32 v239, v146, v239, v78
	ds_read_b32 v216, v238 offset:33792
	ds_read_b32 v217, v239 offset:35840
	v_bfe_u32 v86, v245, 16, 8
	v_lshrrev_b32_e32 v238, 2, v86
	v_and_b32_e32 v239, 15, v86
	v_and_b32_e32 v238, 60, v238
	v_lshlrev_b32_e32 v239, 2, v239
	v_add3_u32 v238, v146, v238, v78
	v_add3_u32 v239, v146, v239, v78
	ds_read_b32 v218, v238 offset:33792
	ds_read_b32 v219, v239 offset:35840
	v_bfe_u32 v85, v245, 24, 8
	v_lshrrev_b32_e32 v238, 2, v85
	v_and_b32_e32 v239, 15, v85
	v_and_b32_e32 v238, 60, v238
	v_lshlrev_b32_e32 v239, 2, v239
	v_add3_u32 v238, v146, v238, v78
	v_add3_u32 v239, v146, v239, v78
	ds_read_b32 v220, v238 offset:33792
	ds_read_b32 v221, v239 offset:35840
	v_bfe_u32 v88, v246, 0, 8
	v_lshrrev_b32_e32 v238, 2, v88
	v_and_b32_e32 v239, 15, v88
	v_and_b32_e32 v238, 60, v238
	v_lshlrev_b32_e32 v239, 2, v239
	v_add3_u32 v238, v146, v238, v78
	v_add3_u32 v239, v146, v239, v78
	ds_read_b32 v222, v238 offset:33792
	ds_read_b32 v223, v239 offset:35840
	v_bfe_u32 v87, v246, 8, 8
	v_lshrrev_b32_e32 v238, 2, v87
	v_and_b32_e32 v239, 15, v87
	v_and_b32_e32 v238, 60, v238
	v_lshlrev_b32_e32 v239, 2, v239
	v_add3_u32 v238, v146, v238, v78
	v_add3_u32 v239, v146, v239, v78
; DI unsigned ordkey(float f) { const unsigned u = __float_as_uint(f); return (u & 0x80000000u) ? ~u : (u | 0x80000000u); }
; DI void peer_select_unit(const Params& p, int unit, char* lds, const bf16x8 (&kb)[4][4]) {
;     ...
;     for (int i = 0; i < 16; ++i) {
;       const unsigned code = PEER_CAND[16 * q4 + i];
;       const float v = topv[tok * 16 + ((code >> 4) & 15)] + topv[(32 + tok) * 16 + (code & 15)];
;       c[i] = code == 0xFFu ? 0u : ((ordkey(v) & ~255u) | (255u - code));
;     }
	ds_read_b32 v224, v238 offset:33792
	ds_read_b32 v225, v239 offset:35840
	v_bfe_u32 v90, v246, 16, 8
	v_lshrrev_b32_e32 v238, 2, v90
	v_and_b32_e32 v239, 15, v90
	v_and_b32_e32 v238, 60, v238
	v_lshlrev_b32_e32 v239, 2, v239
	v_add3_u32 v238, v146, v238, v78
	v_add3_u32 v239, v146, v239, v78
	ds_read_b32 v226, v238 offset:33792
	ds_read_b32 v227, v239 offset:35840
	v_bfe_u32 v89, v246, 24, 8
	v_lshrrev_b32_e32 v238, 2, v89
	v_and_b32_e32 v239, 15, v89
	v_and_b32_e32 v238, 60, v238
	v_lshlrev_b32_e32 v239, 2, v239
	v_add3_u32 v238, v146, v238, v78
	v_add3_u32 v239, v146, v239, v78
	ds_read_b32 v228, v238 offset:33792
	ds_read_b32 v229, v239 offset:35840
	v_bfe_u32 v92, v247, 0, 8
	v_lshrrev_b32_e32 v238, 2, v92
	v_and_b32_e32 v239, 15, v92
	v_and_b32_e32 v238, 60, v238
	v_lshlrev_b32_e32 v239, 2, v239
	v_add3_u32 v238, v146, v238, v78
	v_add3_u32 v239, v146, v239, v78
	ds_read_b32 v230, v238 offset:33792
	ds_read_b32 v231, v239 offset:35840
	v_bfe_u32 v91, v247, 8, 8
	v_lshrrev_b32_e32 v238, 2, v91
	v_and_b32_e32 v239, 15, v91
	v_and_b32_e32 v238, 60, v238
	v_lshlrev_b32_e32 v239, 2, v239
	v_add3_u32 v238, v146, v238, v78
	v_add3_u32 v239, v146, v239, v78
	ds_read_b32 v232, v238 offset:33792
	ds_read_b32 v233, v239 offset:35840
	v_bfe_u32 v94, v247, 16, 8
	v_lshrrev_b32_e32 v238, 2, v94
	v_and_b32_e32 v239, 15, v94
	v_and_b32_e32 v238, 60, v238
	v_lshlrev_b32_e32 v239, 2, v239
	v_add3_u32 v238, v146, v238, v78
	v_add3_u32 v239, v146, v239, v78
	ds_read_b32 v234, v238 offset:33792
	ds_read_b32 v235, v239 offset:35840
	v_bfe_u32 v70, v247, 24, 8
	v_lshrrev_b32_e32 v238, 2, v70
	v_and_b32_e32 v239, 15, v70
	v_and_b32_e32 v238, 60, v238
	v_lshlrev_b32_e32 v239, 2, v239
	v_add3_u32 v238, v146, v238, v78
	v_add3_u32 v239, v146, v239, v78
	ds_read_b32 v236, v238 offset:33792
	ds_read_b32 v237, v239 offset:35840
	s_waitcnt lgkmcnt(0)
	v_add_f32_e32 v210, v210, v211
	v_cmp_gt_i32_e64 s[4:5], 0, v210
	v_not_b32_e32 v211, v210
	v_or_b32_e32 v238, 0x80000000, v210
	v_cndmask_b32_e64 v210, v238, v211, s[4:5]
	v_and_b32_e32 v210, 0xffffff00, v210
	v_bitop3_b32 v82, v210, s19, v82 bitop3:0x36
	v_add_f32_e32 v212, v212, v213
	v_cmp_gt_i32_e64 s[4:5], 0, v212
	v_not_b32_e32 v213, v212
	v_or_b32_e32 v238, 0x80000000, v212
	v_cndmask_b32_e64 v212, v238, v213, s[4:5]
	v_and_b32_e32 v212, 0xffffff00, v212
	v_bitop3_b32 v81, v212, s19, v81 bitop3:0x36
	v_add_f32_e32 v214, v214, v215
	v_cmp_gt_i32_e64 s[4:5], 0, v214
	v_not_b32_e32 v215, v214
	v_or_b32_e32 v238, 0x80000000, v214
	v_cndmask_b32_e64 v214, v238, v215, s[4:5]
	v_and_b32_e32 v214, 0xffffff00, v214
	v_bitop3_b32 v84, v214, s19, v84 bitop3:0x36
	v_add_f32_e32 v216, v216, v217
	v_cmp_gt_i32_e64 s[4:5], 0, v216
	v_not_b32_e32 v217, v216
	v_or_b32_e32 v238, 0x80000000, v216
	v_cndmask_b32_e64 v216, v238, v217, s[4:5]
	v_and_b32_e32 v216, 0xffffff00, v216
	v_bitop3_b32 v83, v216, s19, v83 bitop3:0x36
	v_add_f32_e32 v218, v218, v219
	v_cmp_gt_i32_e64 s[4:5], 0, v218
	v_not_b32_e32 v219, v218
	v_or_b32_e32 v238, 0x80000000, v218
	v_cndmask_b32_e64 v218, v238, v219, s[4:5]
	v_and_b32_e32 v218, 0xffffff00, v218
	v_bitop3_b32 v86, v218, s19, v86 bitop3:0x36
	v_add_f32_e32 v220, v220, v221
	v_cmp_gt_i32_e64 s[4:5], 0, v220
	v_not_b32_e32 v221, v220
	v_or_b32_e32 v238, 0x80000000, v220
	v_cndmask_b32_e64 v220, v238, v221, s[4:5]
	v_and_b32_e32 v220, 0xffffff00, v220
	v_bitop3_b32 v85, v220, s19, v85 bitop3:0x36
	v_add_f32_e32 v222, v222, v223
	v_cmp_gt_i32_e64 s[4:5], 0, v222
	v_not_b32_e32 v223, v222
	v_or_b32_e32 v238, 0x80000000, v222
	v_cndmask_b32_e64 v222, v238, v223, s[4:5]
	v_and_b32_e32 v222, 0xffffff00, v222
	v_bitop3_b32 v88, v222, s19, v88 bitop3:0x36
	v_add_f32_e32 v224, v224, v225
	v_cmp_gt_i32_e64 s[4:5], 0, v224
	v_not_b32_e32 v225, v224
	v_or_b32_e32 v238, 0x80000000, v224
	v_cndmask_b32_e64 v224, v238, v225, s[4:5]
	v_and_b32_e32 v224, 0xffffff00, v224
	v_bitop3_b32 v87, v224, s19, v87 bitop3:0x36
	v_add_f32_e32 v226, v226, v227
	v_cmp_gt_i32_e64 s[4:5], 0, v226
	v_not_b32_e32 v227, v226
	v_or_b32_e32 v238, 0x80000000, v226
	v_cndmask_b32_e64 v226, v238, v227, s[4:5]
	v_and_b32_e32 v226, 0xffffff00, v226
	v_bitop3_b32 v90, v226, s19, v90 bitop3:0x36
	v_add_f32_e32 v228, v228, v229
	v_cmp_gt_i32_e64 s[4:5], 0, v228
	v_not_b32_e32 v229, v228
	v_or_b32_e32 v238, 0x80000000, v228
	v_cndmask_b32_e64 v228, v238, v229, s[4:5]
	v_and_b32_e32 v228, 0xffffff00, v228
	v_bitop3_b32 v89, v228, s19, v89 bitop3:0x36
	v_add_f32_e32 v230, v230, v231
	v_cmp_gt_i32_e64 s[4:5], 0, v230
	v_not_b32_e32 v231, v230
	v_or_b32_e32 v238, 0x80000000, v230
	v_cndmask_b32_e64 v230, v238, v231, s[4:5]
	v_and_b32_e32 v230, 0xffffff00, v230
	v_bitop3_b32 v92, v230, s19, v92 bitop3:0x36
	v_add_f32_e32 v232, v232, v233
	v_cmp_gt_i32_e64 s[4:5], 0, v232
	v_not_b32_e32 v233, v232
	v_or_b32_e32 v238, 0x80000000, v232
	v_cndmask_b32_e64 v232, v238, v233, s[4:5]
	v_and_b32_e32 v232, 0xffffff00, v232
	v_bitop3_b32 v91, v232, s19, v91 bitop3:0x36
	v_add_f32_e32 v234, v234, v235
	v_cmp_gt_i32_e64 s[4:5], 0, v234
	v_not_b32_e32 v235, v234
	v_or_b32_e32 v238, 0x80000000, v234
	v_cndmask_b32_e64 v234, v238, v235, s[4:5]
	v_and_b32_e32 v234, 0xffffff00, v234
	v_bitop3_b32 v94, v234, s19, v94 bitop3:0x36
	v_add_f32_e32 v236, v236, v237
	v_cmp_gt_i32_e64 s[4:5], 0, v236
	v_not_b32_e32 v237, v236
	v_or_b32_e32 v238, 0x80000000, v236
	v_cndmask_b32_e64 v236, v238, v237, s[4:5]
	v_and_b32_e32 v236, 0xffffff00, v236
	v_bitop3_b32 v93, v236, s19, v70 bitop3:0x36
	s_or_b64 exec, exec, s[6:7]
	s_mov_b64 s[4:5], exec
	s_branch .LBB0_1650
